# baseline (speedup 1.0000x reference)
_Z11attn_kernelPKDF16_S0_S0_PfPDF16_S1_:
	s_lshl_b32 s3, s2, 7
	s_lshr_b32 s4, s2, 2
	s_and_b32 s3, s3, 0x180
	s_and_b32 s4, s4, 0x3ffffffe
	s_add_i32 s3, s3, s4
	s_bfe_u32 s2, s2, 0x10002
	s_or_b32 s40, s3, s2
	s_mov_b32 s41, 0
	s_lshl_b64 s[2:3], s[40:41], 2
	s_getpc_b64 s[4:5]
	s_add_u32 s4, s4, g_tab@rel32@lo+4
	s_addc_u32 s5, s5, g_tab@rel32@hi+12
	s_add_u32 s42, s4, s2
	s_addc_u32 s43, s5, s3
	s_load_dword s12, s[42:43], 0x0
	s_load_dwordx4 s[4:7], s[0:1], 0x8
	s_load_dword s76, s[42:43], 0x1000
	s_load_dwordx2 s[80:81], s[0:1], 0x0
	s_load_dwordx4 s[84:87], s[0:1], 0x18
	s_load_dwordx2 s[88:89], s[0:1], 0x28
	v_lshlrev_b32_e32 v2, 4, v0
	s_movk_i32 s8, 0x70
	v_readfirstlane_b32 s3, v0
	s_waitcnt lgkmcnt(0)
	s_add_u32 s70, s4, 0x2000
	s_addc_u32 s71, s5, 0
	s_add_u32 s72, s6, 0x2000
	s_addc_u32 s73, s7, 0
	s_and_b32 s2, s12, 3
	s_lshl_b32 s10, s2, 19
	v_bitop3_b32 v10, v2, s8, v0 bitop3:0x48
	s_add_u32 s8, s6, s10
	s_addc_u32 s9, s7, 0
	s_lshr_b32 s13, s3, 6
	s_bfe_u32 s40, s12, 0x70007
	s_bfe_u32 s33, s12, 0x6000e
	v_and_b32_e32 v1, 0x1f80, v2
	s_add_u32 s10, s4, s10
	v_or_b32_e32 v50, v10, v1
	v_mov_b32_e32 v51, 0
	s_addc_u32 s11, s5, 0
	v_lshl_add_u64 v[52:53], s[10:11], 0, v[50:51]
	v_lshl_add_u64 v[54:55], s[8:9], 0, v[50:51]
	s_lshl_b32 s8, s40, 13
	s_mov_b32 s9, s41
	s_lshl_b32 s50, s13, 10
	v_lshl_add_u64 v[2:3], v[52:53], 0, s[8:9]
	s_mov_b32 m0, s50
	s_add_i32 s51, s50, 0x2000
	global_load_lds_dwordx4 v[2:3], off
	v_lshl_add_u64 v[2:3], v[54:55], 0, s[8:9]
	s_mov_b32 m0, s51
	s_cmp_eq_u32 s33, 0
	global_load_lds_dwordx4 v[2:3], off
	s_cbranch_scc1 .LBB2_30
	s_mov_b64 s[14:15], s[80:81]
	s_mov_b64 s[8:9], s[84:85]
	s_mov_b64 s[10:11], s[86:87]
	s_mov_b64 s[44:45], s[88:89]
	s_cmp_lt_u32 s13, 4
	s_cbranch_scc1 .Lattn_prio_done
	s_setprio 3
